# LDS-DMA gather with 40 KB static LDS per workgroup (4 workgroups per CU instead of 5)
# speedup vs baseline: 1.0195x; 1.0191x over previous
	.amdhsa_kernel _Z13gather_kernelPKDv2_DF16_PKiPf
		.amdhsa_group_segment_fixed_size 40960
		.amdhsa_private_segment_fixed_size 0
		.amdhsa_kernarg_size 24
		.amdhsa_user_sgpr_count 2
		.amdhsa_user_sgpr_dispatch_ptr 0
		.amdhsa_user_sgpr_queue_ptr 0
		.amdhsa_user_sgpr_kernarg_segment_ptr 1
		.amdhsa_user_sgpr_dispatch_id 0
		.amdhsa_user_sgpr_kernarg_preload_length 0
		.amdhsa_user_sgpr_kernarg_preload_offset 0
		.amdhsa_user_sgpr_private_segment_size 0
		.amdhsa_uses_dynamic_stack 0
		.amdhsa_enable_private_segment 0
		.amdhsa_system_sgpr_workgroup_id_x 1
		.amdhsa_system_sgpr_workgroup_id_y 0
		.amdhsa_system_sgpr_workgroup_id_z 0
		.amdhsa_system_sgpr_workgroup_info 0
		.amdhsa_system_vgpr_workitem_id 0
		.amdhsa_next_free_vgpr 64
		.amdhsa_next_free_sgpr 16
		.amdhsa_accum_offset 64
		.amdhsa_reserve_vcc 0
		.amdhsa_float_round_mode_32 0
		.amdhsa_float_round_mode_16_64 0
		.amdhsa_float_denorm_mode_32 3
		.amdhsa_float_denorm_mode_16_64 3
		.amdhsa_dx10_clamp 1
		.amdhsa_ieee_mode 1
		.amdhsa_fp16_overflow 0
		.amdhsa_tg_split 0
		.amdhsa_exception_fp_ieee_invalid_op 0
		.amdhsa_exception_fp_denorm_src 0
		.amdhsa_exception_fp_ieee_div_zero 0
		.amdhsa_exception_fp_ieee_overflow 0
		.amdhsa_exception_fp_ieee_underflow 0
		.amdhsa_exception_fp_ieee_inexact 0
		.amdhsa_exception_int_div_zero 0
	.end_amdhsa_kernel

amdhsa.kernels:
  - .agpr_count:     0
    .args:
      - .actual_access:  read_only
        .address_space:  global
        .offset:         0
        .size:           8
        .value_kind:     global_buffer
      - .actual_access:  write_only
        .address_space:  global
        .offset:         8
        .size:           8
        .value_kind:     global_buffer
    .group_segment_fixed_size: 0
    .kernarg_segment_align: 8
    .kernarg_segment_size: 16
    .language:       OpenCL C
    .language_version:
      - 2
      - 0
    .max_flat_workgroup_size: 256
    .name:           _Z10cvt_kernelPKDv4_fPDv4_DF16_
    .private_segment_fixed_size: 0
    .sgpr_count:     24
    .sgpr_spill_count: 0
    .symbol:         _Z10cvt_kernelPKDv4_fPDv4_DF16_.kd
    .uniform_work_group_size: 1
    .uses_dynamic_stack: false
    .vgpr_count:     38
    .vgpr_spill_count: 0
    .wavefront_size: 64
  - .agpr_count:     0
    .args:
      - .actual_access:  read_only
        .address_space:  global
        .offset:         0
        .size:           8
        .value_kind:     global_buffer
      - .actual_access:  read_only
        .address_space:  global
        .offset:         8
        .size:           8
        .value_kind:     global_buffer
      - .actual_access:  write_only
        .address_space:  global
        .offset:         16
        .size:           8
        .value_kind:     global_buffer
    .group_segment_fixed_size: 40960
    .kernarg_segment_align: 8
    .kernarg_segment_size: 24
    .language:       OpenCL C
    .language_version:
      - 2
      - 0
    .max_flat_workgroup_size: 256
    .name:           _Z13gather_kernelPKDv2_DF16_PKiPf
    .private_segment_fixed_size: 0
    .sgpr_count:     22
    .sgpr_spill_count: 0
    .symbol:         _Z13gather_kernelPKDv2_DF16_PKiPf.kd
    .uniform_work_group_size: 1
    .uses_dynamic_stack: false
    .vgpr_count:     64
    .vgpr_spill_count: 0
    .wavefront_size: 64
